# MoE gather row copy: the four rows of a group are loaded together with their scales and then stored (was load-wait-store per row); on top of the N1 batching variant
# baseline (speedup 1.0000x reference)
.LBB0_1406:
	s_add_i32 s52, s50, s51
	s_ashr_i32 s0, s52, 1
	s_add_i32 s4, s0, s71
	s_ashr_i32 s5, s4, 31
	s_lshl_b64 s[0:1], s[4:5], 10
	v_lshl_add_u64 v[12:13], v[8:9], 0, s[0:1]
	global_load_dwordx4 v[28:31], v[12:13], off
	s_lshl_b64 s[4:5], s[4:5], 2
	s_add_u32 s4, s88, s4
	s_addc_u32 s5, s89, s5
	global_load_dword v44, v67, s[4:5]
	s_add_i32 s0, s52, 1
	s_ashr_i32 s0, s0, 1
	s_add_i32 s4, s0, s71
	s_ashr_i32 s5, s4, 31
	s_lshl_b64 s[0:1], s[4:5], 10
	v_lshl_add_u64 v[12:13], v[8:9], 0, s[0:1]
	global_load_dwordx4 v[32:35], v[12:13], off
	s_lshl_b64 s[4:5], s[4:5], 2
	s_add_u32 s4, s88, s4
	s_addc_u32 s5, s89, s5
	global_load_dword v45, v67, s[4:5]
	s_add_i32 s0, s52, 2
	s_ashr_i32 s0, s0, 1
	s_add_i32 s4, s0, s71
	s_ashr_i32 s5, s4, 31
	s_lshl_b64 s[0:1], s[4:5], 10
	v_lshl_add_u64 v[12:13], v[8:9], 0, s[0:1]
	global_load_dwordx4 v[36:39], v[12:13], off
	s_lshl_b64 s[4:5], s[4:5], 2
	s_add_u32 s4, s88, s4
	s_addc_u32 s5, s89, s5
	global_load_dword v46, v67, s[4:5]
	s_add_i32 s0, s52, 3
	s_ashr_i32 s0, s0, 1
	s_add_i32 s4, s0, s71
	s_ashr_i32 s5, s4, 31
	s_lshl_b64 s[0:1], s[4:5], 10
	v_lshl_add_u64 v[12:13], v[8:9], 0, s[0:1]
	global_load_dwordx4 v[40:43], v[12:13], off
	s_lshl_b64 s[4:5], s[4:5], 2
	s_add_u32 s4, s88, s4
	s_addc_u32 s5, s89, s5
	global_load_dword v47, v67, s[4:5]
	ds_read_b32 v22, v20
	ds_read_b32 v23, v20 offset:4
	ds_read_b32 v24, v20 offset:8
	ds_read_b32 v25, v20 offset:12
	s_waitcnt lgkmcnt(0)
	v_ashrrev_i32_e32 v13, 31, v22
	v_mov_b32_e32 v12, v22
	v_lshlrev_b64 v[26:27], 10, v[12:13]
	v_lshl_add_u64 v[26:27], v[10:11], 0, v[26:27]
	v_ashrrev_i32_e32 v13, 31, v23
	v_mov_b32_e32 v12, v23
	v_lshlrev_b64 v[48:49], 10, v[12:13]
	v_lshl_add_u64 v[48:49], v[10:11], 0, v[48:49]
	v_ashrrev_i32_e32 v13, 31, v24
	v_mov_b32_e32 v12, v24
	v_lshlrev_b64 v[68:69], 10, v[12:13]
	v_lshl_add_u64 v[68:69], v[10:11], 0, v[68:69]
	v_ashrrev_i32_e32 v13, 31, v25
	v_mov_b32_e32 v12, v25
	v_lshlrev_b64 v[70:71], 10, v[12:13]
	v_lshl_add_u64 v[70:71], v[10:11], 0, v[70:71]
	s_waitcnt vmcnt(0)
	global_store_dwordx4 v[26:27], v[28:31], off
	global_store_dwordx4 v[48:49], v[32:35], off
	global_store_dwordx4 v[68:69], v[36:39], off
	global_store_dwordx4 v[70:71], v[40:43], off
	s_and_saveexec_b64 s[0:1], s[44:45]
	v_ashrrev_i32_e32 v13, 31, v22
	v_mov_b32_e32 v12, v22
	v_lshlrev_b64 v[12:13], 2, v[12:13]
	v_lshl_add_u64 v[26:27], s[68:69], 0, v[12:13]
	global_store_dword v[26:27], v44, off
	v_ashrrev_i32_e32 v13, 31, v23
	v_mov_b32_e32 v12, v23
	v_lshlrev_b64 v[12:13], 2, v[12:13]
	v_lshl_add_u64 v[48:49], s[68:69], 0, v[12:13]
	global_store_dword v[48:49], v45, off
	v_ashrrev_i32_e32 v13, 31, v24
	v_mov_b32_e32 v12, v24
	v_lshlrev_b64 v[12:13], 2, v[12:13]
	v_lshl_add_u64 v[68:69], s[68:69], 0, v[12:13]
	global_store_dword v[68:69], v46, off
	v_ashrrev_i32_e32 v13, 31, v25
	v_mov_b32_e32 v12, v25
	v_lshlrev_b64 v[12:13], 2, v[12:13]
	v_lshl_add_u64 v[70:71], s[68:69], 0, v[12:13]
	global_store_dword v[70:71], v47, off
	s_or_b64 exec, exec, s[0:1]
	s_add_i32 s51, s51, 4
	s_cmp_eq_u32 s51, 16
	v_add_u32_e32 v20, 16, v20
	s_cbranch_scc1 .LBB0_1348
	s_branch .LBB0_1406
